# k_agg1: last xnack-only s_nop pad in the main gather path removed
# baseline (speedup 1.0000x reference)
.Lagg_full:
	global_load_dwordx4 v[30:33], v[2:3], off
	v_add_u32_e32 v0, 8, v0
	v_cmp_ge_i32_e64 s[18:19], v0, v1
	v_lshl_add_u64 v[2:3], v[2:3], 0, 16
	s_or_b64 s[30:31], s[18:19], s[30:31]
	s_waitcnt vmcnt(0)
	v_mad_u32_u16 v39, v30, s34, v6
	v_mad_u32_u16 v38, v30, s34, v6 op_sel:[1,0,0,0]
	v_mad_u32_u16 v40, v31, s34, v6
	v_mad_u32_u16 v42, v31, s34, v6 op_sel:[1,0,0,0]
	v_mad_u32_u16 v46, v32, s34, v6
	v_mad_u32_u16 v50, v32, s34, v6 op_sel:[1,0,0,0]
	v_mad_u32_u16 v54, v33, s34, v6
	v_mad_u32_u16 v58, v33, s34, v6 op_sel:[1,0,0,0]
	global_load_dwordx4 v[30:33], v39, s[20:21]
	global_load_dwordx4 v[34:37], v38, s[20:21]
	global_load_dwordx4 v[38:41], v40, s[20:21]
	global_load_dwordx4 v[42:45], v42, s[20:21]
	global_load_dwordx4 v[46:49], v46, s[20:21]
	global_load_dwordx4 v[50:53], v50, s[20:21]
	global_load_dwordx4 v[54:57], v54, s[20:21]
	global_load_dwordx4 v[58:61], v58, s[20:21]
	s_waitcnt vmcnt(6)
	v_pk_add_f16 v33, v33, v37
	v_pk_add_f16 v32, v32, v36
	v_pk_add_f16 v31, v31, v35
	v_pk_add_f16 v30, v30, v34
	s_waitcnt vmcnt(4)
	v_pk_add_f16 v34, v41, v45
	v_pk_add_f16 v35, v40, v44
	v_pk_add_f16 v36, v39, v43
	v_pk_add_f16 v37, v38, v42
	s_waitcnt vmcnt(2)
	v_pk_add_f16 v38, v49, v53
	v_pk_add_f16 v39, v48, v52
	v_pk_add_f16 v40, v47, v51
	v_pk_add_f16 v41, v46, v50
	s_waitcnt vmcnt(0)
	v_pk_add_f16 v42, v57, v61
	v_pk_add_f16 v43, v56, v60
	v_pk_add_f16 v44, v55, v59
	v_pk_add_f16 v45, v54, v58
	v_pk_add_f16 v30, v30, v37
	v_pk_add_f16 v31, v31, v36
	v_pk_add_f16 v32, v32, v35
	v_pk_add_f16 v33, v33, v34
	v_pk_add_f16 v34, v41, v45
	v_pk_add_f16 v35, v40, v44
	v_pk_add_f16 v36, v39, v43
	v_pk_add_f16 v37, v38, v42
	v_pk_add_f16 v36, v32, v36
	v_pk_add_f16 v37, v33, v37
	v_pk_add_f16 v33, v31, v35
	v_pk_add_f16 v31, v30, v34
	v_cvt_f32_f16_e32 v32, v33
	v_cvt_f32_f16_e32 v30, v31
	v_cvt_f32_f16_sdwa v31, v31 dst_sel:DWORD dst_unused:UNUSED_PAD src0_sel:WORD_1
	v_cvt_f32_f16_sdwa v33, v33 dst_sel:DWORD dst_unused:UNUSED_PAD src0_sel:WORD_1
	v_cvt_f32_f16_e32 v34, v36
	v_cvt_f32_f16_sdwa v35, v36 dst_sel:DWORD dst_unused:UNUSED_PAD src0_sel:WORD_1
	v_cvt_f32_f16_e32 v36, v37
	v_cvt_f32_f16_sdwa v37, v37 dst_sel:DWORD dst_unused:UNUSED_PAD src0_sel:WORD_1
	v_pk_add_f32 v[18:19], v[18:19], v[30:31]
	v_pk_add_f32 v[16:17], v[16:17], v[32:33]
	v_pk_add_f32 v[14:15], v[14:15], v[34:35]
	v_pk_add_f32 v[12:13], v[12:13], v[36:37]
	s_andn2_b64 exec, exec, s[30:31]
	s_cbranch_execnz .LBB3_4
	s_branch .Lagg_loop_done
